# scope split A: prep stores sc1 (agent), fold stores sc0 sc1 (system)
# speedup vs baseline: 1.0122x; 1.0036x over previous
.LBB1_65:
	s_or_b64 exec, exec, s[10:11]
	v_lshrrev_b32_e32 v20, 2, v58
	v_and_b32_e32 v19, 2, v52
	v_and_b32_e32 v20, 28, v20
	v_or_b32_e32 v21, 0x1880, v20
	v_lshlrev_b32_e32 v24, 5, v19
	v_or_b32_e32 v25, v21, v24
	s_waitcnt lgkmcnt(0)
	s_barrier
	ds_read_b32 v25, v25
	v_or_b32_e32 v26, 1, v52
	v_or_b32_e32 v20, 0x1800, v20
	v_lshlrev_b32_e32 v27, 5, v26
	v_or_b32_e32 v24, v20, v24
	v_or_b32_e32 v21, v21, v27
	v_or_b32_e32 v20, v20, v27
	ds_read_b32 v24, v24
	ds_read_b32 v21, v21
	ds_read_b32 v20, v20
	v_lshlrev_b32_e32 v22, 2, v58
	v_or_b32_e32 v23, 0x800, v22
	s_waitcnt vmcnt(1) lgkmcnt(3)
	v_mul_f32_e32 v25, v57, v25
	v_lshlrev_b32_e32 v19, 9, v19
	s_load_dwordx2 s[0:1], s[0:1], 0x48
	v_or_b32_e32 v27, v22, v19
	s_waitcnt vmcnt(0) lgkmcnt(0)
	v_fma_f32 v24, -v25, v24, v56
	v_or_b32_e32 v19, v23, v19
	ds_write_b32 v19, v24
	v_mul_f32_e32 v19, v57, v21
	v_lshlrev_b32_e32 v21, 9, v26
	v_or_b32_e32 v22, v22, v21
	v_and_b32_e32 v48, 63, v0
	ds_write_b32 v22, v19
	v_fma_f32 v19, -v19, v20, v56
	v_or_b32_e32 v20, v23, v21
	ds_write_b32 v20, v19
	v_add_u32_e32 v38, v52, v18
	v_lshlrev_b32_e32 v18, 4, v48
	v_mov_b32_e32 v19, 0
	v_lshl_add_u64 v[40:41], s[0:1], 0, v[18:19]
	v_or_b32_e32 v18, v55, v54
	v_lshlrev_b32_e32 v49, 2, v18
	v_ashrrev_i32_e32 v39, 31, v38
	ds_write_b32 v27, v25
	s_waitcnt lgkmcnt(0)
	s_barrier
	ds_read_b128 v[18:21], v49
	v_lshlrev_b64 v[22:23], 10, v[38:39]
	v_lshl_add_u64 v[42:43], v[40:41], 0, v[22:23]
	ds_read_b128 v[22:25], v49 offset:16
	s_lshl_b32 s5, s4, 2
	s_waitcnt lgkmcnt(1)
	v_pk_mul_f32 v[18:19], v[14:15], v[18:19]
	v_pk_mul_f32 v[20:21], v[16:17], v[20:21]
	s_ashr_i32 s13, s2, 31
	v_cvt_pk_bf16_f32 v18, v18, v19
	v_cvt_pk_bf16_f32 v19, v20, v21
	s_waitcnt lgkmcnt(0)
	v_pk_mul_f32 v[20:21], v[6:7], v[22:23]
	v_pk_mul_f32 v[22:23], v[8:9], v[24:25]
	s_mul_i32 s0, s4, 0xc0
	v_cvt_pk_bf16_f32 v20, v20, v21
	v_cvt_pk_bf16_f32 v21, v22, v23
	s_mul_hi_i32 s1, s5, 48
	s_add_u32 s0, s0, s2
	ds_read_b128 v[22:25], v49 offset:2048
	s_addc_u32 s1, s1, s13
	s_lshl_b64 s[0:1], s[0:1], 15
	v_lshl_add_u64 v[26:27], v[42:43], 0, s[0:1]
	global_store_dwordx4 v[26:27], v[18:21], off sc0 sc1
	ds_read_b128 v[18:21], v49 offset:2064
	s_waitcnt lgkmcnt(1)
	v_mul_f32_e32 v26, v15, v23
	v_fmac_f32_e32 v26, v14, v22
	v_fmac_f32_e32 v26, v16, v24
	v_fmac_f32_e32 v26, v17, v25
	s_waitcnt lgkmcnt(0)
	v_fmac_f32_e32 v26, v6, v18
	v_fmac_f32_e32 v26, v7, v19
	v_fmac_f32_e32 v26, v8, v20
	ds_read_b128 v[22:25], v49 offset:512
	v_fmac_f32_e32 v26, v9, v21
	ds_read_b128 v[18:21], v49 offset:528
	s_or_b32 s6, s5, 1
	s_mul_hi_i32 s7, s6, 48
	s_mul_i32 s6, s6, 48
	s_add_u32 s6, s6, s2
	s_waitcnt lgkmcnt(1)
	v_pk_mul_f32 v[22:23], v[14:15], v[22:23]
	v_pk_mul_f32 v[24:25], v[16:17], v[24:25]
	s_waitcnt lgkmcnt(0)
	v_pk_mul_f32 v[18:19], v[6:7], v[18:19]
	s_addc_u32 s7, s7, s13
	v_cvt_pk_bf16_f32 v22, v22, v23
	v_cvt_pk_bf16_f32 v23, v24, v25
	v_cvt_pk_bf16_f32 v24, v18, v19
	v_pk_mul_f32 v[18:19], v[8:9], v[20:21]
	s_lshl_b64 s[6:7], s[6:7], 15
	v_cvt_pk_bf16_f32 v25, v18, v19
	v_lshl_add_u64 v[18:19], v[42:43], 0, s[6:7]
	v_add_f32_e32 v50, 0, v26
	ds_read_b128 v[26:29], v49 offset:1024
	global_store_dwordx4 v[18:19], v[22:25], off sc0 sc1
	ds_read_b128 v[22:25], v49 offset:2560
	ds_read_b128 v[18:21], v49 offset:2576
	ds_read_b128 v[30:33], v49 offset:1040
	s_or_b32 s10, s5, 2
	s_mul_hi_i32 s11, s10, 48
	s_mul_i32 s10, s10, 48
	s_add_u32 s10, s10, s2
	s_waitcnt lgkmcnt(3)
	v_pk_mul_f32 v[26:27], v[14:15], v[26:27]
	v_pk_mul_f32 v[28:29], v[16:17], v[28:29]
	s_addc_u32 s11, s11, s13
	v_cvt_pk_bf16_f32 v26, v26, v27
	v_cvt_pk_bf16_f32 v27, v28, v29
	s_waitcnt lgkmcnt(0)
	v_pk_mul_f32 v[28:29], v[6:7], v[30:31]
	v_pk_mul_f32 v[30:31], v[8:9], v[32:33]
	s_lshl_b64 s[10:11], s[10:11], 15
	v_cvt_pk_bf16_f32 v28, v28, v29
	v_cvt_pk_bf16_f32 v29, v30, v31
	v_lshl_add_u64 v[34:35], v[42:43], 0, s[10:11]
	ds_read_b128 v[30:33], v49 offset:1536
	global_store_dwordx4 v[34:35], v[26:29], off sc0 sc1
	ds_read_b128 v[26:29], v49 offset:1552
	s_or_b32 s5, s5, 3
	s_mul_hi_i32 s14, s5, 48
	s_mul_i32 s5, s5, 48
	s_add_u32 s12, s5, s2
	s_addc_u32 s13, s14, s13
	s_waitcnt lgkmcnt(1)
	v_pk_mul_f32 v[30:31], v[14:15], v[30:31]
	v_pk_mul_f32 v[32:33], v[16:17], v[32:33]
	s_waitcnt lgkmcnt(0)
	v_pk_mul_f32 v[26:27], v[6:7], v[26:27]
	v_pk_mul_f32 v[44:45], v[8:9], v[28:29]
	s_lshl_b64 s[12:13], s[12:13], 15
	v_add_u32_e32 v38, 4, v38
	v_cvt_pk_bf16_f32 v34, v30, v31
	v_cvt_pk_bf16_f32 v35, v32, v33
	v_cvt_pk_bf16_f32 v36, v26, v27
	v_cvt_pk_bf16_f32 v37, v44, v45
	v_lshl_add_u64 v[42:43], v[42:43], 0, s[12:13]
	v_add_lshl_u32 v71, v55, v54, 2
	v_ashrrev_i32_e32 v39, 31, v38
	ds_read_b128 v[30:33], v49 offset:3072
	ds_read_b128 v[26:29], v49 offset:3088
	global_store_dwordx4 v[42:43], v[34:37], off sc0 sc1
	ds_read_b128 v[34:37], v71 offset:256
	v_lshlrev_b64 v[38:39], 10, v[38:39]
	v_lshl_add_u64 v[46:47], v[40:41], 0, v[38:39]
	ds_read_b128 v[38:41], v71 offset:272
	v_lshlrev_b32_e32 v66, 2, v53
	s_waitcnt lgkmcnt(1)
	v_pk_mul_f32 v[34:35], v[10:11], v[34:35]
	v_pk_mul_f32 v[36:37], v[12:13], v[36:37]
	v_cvt_pk_bf16_f32 v34, v34, v35
	v_cvt_pk_bf16_f32 v35, v36, v37
	s_waitcnt lgkmcnt(0)
	v_pk_mul_f32 v[36:37], v[2:3], v[38:39]
	v_pk_mul_f32 v[42:43], v[4:5], v[40:41]
	ds_read_b128 v[38:41], v71 offset:2304
	v_cvt_pk_bf16_f32 v36, v36, v37
	v_cvt_pk_bf16_f32 v37, v42, v43
	v_lshl_add_u64 v[42:43], v[46:47], 0, s[0:1]
	global_store_dwordx4 v[42:43], v[34:37], off sc0 sc1
	ds_read_b128 v[34:37], v71 offset:2320
	s_waitcnt lgkmcnt(1)
	v_mul_f32_e32 v51, v11, v39
	v_fmac_f32_e32 v51, v10, v38
	v_fmac_f32_e32 v51, v12, v40
	v_fmac_f32_e32 v51, v13, v41
	s_waitcnt lgkmcnt(0)
	v_fmac_f32_e32 v51, v2, v34
	v_fmac_f32_e32 v51, v3, v35
	v_fmac_f32_e32 v51, v4, v36
	ds_read_b128 v[38:41], v71 offset:768
	v_fmac_f32_e32 v51, v5, v37
	ds_read_b128 v[34:37], v71 offset:784
	s_movk_i32 s0, 0x1000
	v_add_f32_e32 v69, v50, v51
	s_waitcnt lgkmcnt(1)
	v_pk_mul_f32 v[38:39], v[10:11], v[38:39]
	v_pk_mul_f32 v[40:41], v[12:13], v[40:41]
	s_waitcnt lgkmcnt(0)
	v_pk_mul_f32 v[34:35], v[2:3], v[34:35]
	v_pk_mul_f32 v[42:43], v[4:5], v[36:37]
	v_cvt_pk_bf16_f32 v38, v38, v39
	v_cvt_pk_bf16_f32 v39, v40, v41
	v_cvt_pk_bf16_f32 v40, v34, v35
	ds_read_b128 v[34:37], v71 offset:1280
	v_cvt_pk_bf16_f32 v41, v42, v43
	v_lshl_add_u64 v[42:43], v[46:47], 0, s[6:7]
	global_store_dwordx4 v[42:43], v[38:41], off sc0 sc1
	ds_read_b128 v[38:41], v71 offset:1296
	s_waitcnt lgkmcnt(1)
	v_pk_mul_f32 v[34:35], v[10:11], v[34:35]
	v_pk_mul_f32 v[36:37], v[12:13], v[36:37]
	v_cvt_pk_bf16_f32 v34, v34, v35
	v_cvt_pk_bf16_f32 v35, v36, v37
	s_waitcnt lgkmcnt(0)
	v_pk_mul_f32 v[36:37], v[2:3], v[38:39]
	v_pk_mul_f32 v[42:43], v[4:5], v[40:41]
	v_cvt_pk_bf16_f32 v36, v36, v37
	v_cvt_pk_bf16_f32 v37, v42, v43
	v_lshl_add_u64 v[42:43], v[46:47], 0, s[10:11]
	ds_read_b128 v[38:41], v71 offset:1792
	global_store_dwordx4 v[42:43], v[34:37], off sc0 sc1
	ds_read_b128 v[34:37], v71 offset:1808
	v_lshl_add_u64 v[46:47], v[46:47], 0, s[12:13]
	s_waitcnt lgkmcnt(1)
	v_pk_mul_f32 v[38:39], v[10:11], v[38:39]
	v_pk_mul_f32 v[40:41], v[12:13], v[40:41]
	s_waitcnt lgkmcnt(0)
	v_pk_mul_f32 v[34:35], v[2:3], v[34:35]
	v_cvt_pk_bf16_f32 v42, v38, v39
	v_cvt_pk_bf16_f32 v44, v34, v35
	v_pk_mul_f32 v[34:35], v[4:5], v[36:37]
	v_cvt_pk_bf16_f32 v43, v40, v41
	v_cvt_pk_bf16_f32 v45, v34, v35
	ds_read_b128 v[38:41], v49 offset:3584
	ds_read_b128 v[34:37], v49 offset:3600
	global_store_dwordx4 v[46:47], v[42:45], off sc0 sc1
	s_nop 1
	v_mbcnt_lo_u32_b32 v42, -1, 0
	v_mbcnt_hi_u32_b32 v42, -1, v42
	v_and_b32_e32 v44, 64, v42
	v_xor_b32_e32 v43, 32, v42
	v_add_u32_e32 v44, 64, v44
	v_cmp_lt_i32_e32 vcc, v43, v44
	s_nop 1
	v_cndmask_b32_e32 v42, v42, v43, vcc
	v_lshlrev_b32_e32 v68, 2, v42
	v_lshlrev_b32_e32 v42, 9, v52
	v_cmp_gt_u32_e32 vcc, 32, v48
	v_or3_b32 v67, v42, v66, s0
	ds_read_b128 v[62:65], v71 offset:2816
	ds_read_b128 v[58:61], v71 offset:2832
	ds_read_b128 v[54:57], v71 offset:3328
	ds_read_b128 v[50:53], v71 offset:3344
	ds_read_b128 v[46:49], v71 offset:3840
	ds_read_b128 v[42:45], v71 offset:3856
	ds_bpermute_b32 v70, v68, v69
	s_and_saveexec_b64 s[0:1], vcc
	s_cbranch_execz .LBB1_67
	s_waitcnt lgkmcnt(0)
	v_add_f32_e32 v69, v69, v70
	ds_write_b32 v67, v69
